# speedup vs baseline: 1.0036x; 1.0036x over previous
.LBB0_3:
	s_load_dwordx8 s[20:27], s[0:1], 0x68
	s_load_dwordx4 s[40:43], s[0:1], 0x0
	s_load_dwordx2 s[44:45], s[0:1], 0x10
	v_and_b32_e32 v2, 31, v0
	s_lshr_b32 s3, s2, 3
	s_and_b32 s30, s2, 7
	v_cmp_gt_u32_e64 s[10:11], 21, v2
	s_mul_i32 s30, s30, 0x30000
	v_lshrrev_b32_e32 v6, 5, v0
	v_cndmask_b32_e64 v1, 0, v2, s[10:11]
	s_cmpk_gt_u32 s2, 0x41f
	s_cbranch_scc0 .LBB0_11
	s_cmpk_gt_u32 s2, 0x45f
	s_cbranch_scc0 .LBB0_8
	s_load_dwordx2 s[28:29], s[0:1], 0x60
	s_load_dwordx2 s[18:19], s[0:1], 0x48
	s_load_dwordx2 s[8:9], s[0:1], 0x38
	s_load_dwordx2 s[32:33], s[0:1], 0x40
	s_load_dwordx4 s[36:39], s[0:1], 0x50
	v_lshrrev_b32_e32 v3, 2, v2
	v_and_b32_e32 v2, 28, v2
	v_and_b32_e32 v7, 3, v0
	v_and_b32_e32 v51, 7, v0
	v_lshlrev_b32_e32 v51, 2, v51
	s_waitcnt lgkmcnt(0)
	global_load_dword v52, v51, s[28:29]
	global_load_dword v53, v51, s[32:33]
	global_load_dword v54, v51, s[38:39]
	global_load_dword v55, v51, s[36:37]
	global_load_dword v51, v51, s[18:19]
	global_load_dword v22, v2, s[18:19]
	global_load_dword v23, v2, s[28:29]
	v_cmp_lt_u32_e32 vcc, 31, v0
	v_mul_u32_u24_e32 v24, 27, v3
	v_sub_u32_e32 v27, 2, v7
	v_cndmask_b32_e64 v2, 0, 1, vcc
	v_sub_co_u32_e32 v26, vcc, 1, v7
	v_max_i32_e32 v8, 0, v26
	v_lshl_add_u32 v8, v8, 3, v8
	v_sub_u32_e32 v16, 4, v7
	v_add_lshl_u32 v4, v24, v2, 2
	v_mov_b32_e32 v5, 0
	v_ashrrev_i32_e32 v9, 31, v8
	v_max_i32_e32 v12, 0, v27
	v_min_u32_e32 v16, 2, v16
	v_lshl_add_u64 v[2:3], s[8:9], 0, v[4:5]
	v_lshlrev_b64 v[8:9], 2, v[8:9]
	v_mul_u32_u24_e32 v12, 9, v12
	v_mul_u32_u24_e32 v16, 9, v16
	v_lshl_add_u64 v[10:11], v[2:3], 0, v[8:9]
	v_lshlrev_b32_e32 v12, 2, v12
	v_mov_b32_e32 v13, v5
	v_lshlrev_b32_e32 v16, 2, v16
	v_mov_b32_e32 v17, v5
	global_load_dword v25, v4, s[8:9]
	v_lshl_add_u64 v[14:15], v[2:3], 0, v[12:13]
	v_lshl_add_u64 v[18:19], v[2:3], 0, v[16:17]
	global_load_dword v28, v[10:11], off
	global_load_dword v29, v[14:15], off
	global_load_dword v30, v[18:19], off
	v_bitop3_b32 v10, v0, 3, v0 bitop3:0xc
	v_min_u32_e32 v10, 2, v10
	v_mul_u32_u24_e32 v10, 9, v10
	v_lshlrev_b32_e32 v10, 2, v10
	v_mov_b32_e32 v11, v5
	v_lshl_add_u64 v[2:3], v[2:3], 0, v[10:11]
	v_cmp_gt_u32_e64 s[4:5], 32, v0
	global_load_dword v31, v[2:3], off
	global_load_dword v32, v4, s[8:9] offset:72
	v_cndmask_b32_e64 v2, 4, 3, s[4:5]
	v_add_lshl_u32 v4, v2, v24, 2
	v_lshl_add_u64 v[2:3], s[8:9], 0, v[4:5]
	v_lshl_add_u64 v[14:15], v[2:3], 0, v[8:9]
	global_load_dword v33, v4, s[8:9]
	global_load_dword v34, v[14:15], off
	v_lshl_add_u64 v[14:15], v[2:3], 0, v[12:13]
	v_lshl_add_u64 v[18:19], v[2:3], 0, v[10:11]
	v_lshl_add_u64 v[2:3], v[2:3], 0, v[16:17]
	global_load_dword v35, v[14:15], off
	global_load_dword v36, v[18:19], off
	global_load_dword v37, v[2:3], off
	global_load_dword v38, v4, s[8:9] offset:72
	v_cndmask_b32_e64 v2, 8, 7, s[4:5]
	v_add_lshl_u32 v4, v2, v24, 2
	v_lshl_add_u64 v[2:3], s[8:9], 0, v[4:5]
	v_lshl_add_u64 v[14:15], v[2:3], 0, v[8:9]
	v_lshl_add_u64 v[18:19], v[2:3], 0, v[12:13]
	v_lshl_add_u64 v[20:21], v[2:3], 0, v[10:11]
	v_lshl_add_u64 v[2:3], v[2:3], 0, v[16:17]
	global_load_dword v39, v4, s[8:9]
	global_load_dword v40, v[14:15], off
	global_load_dword v41, v[18:19], off
	global_load_dword v42, v[20:21], off
	global_load_dword v43, v[2:3], off
	global_load_dword v44, v4, s[8:9] offset:72
	v_cndmask_b32_e64 v2, 5, 2, s[4:5]
	v_add_lshl_u32 v4, v2, v24, 2
	v_lshl_add_u64 v[2:3], s[8:9], 0, v[4:5]
	v_lshl_add_u64 v[14:15], v[2:3], 0, v[8:9]
	v_lshl_add_u64 v[18:19], v[2:3], 0, v[12:13]
	v_lshl_add_u64 v[20:21], v[2:3], 0, v[10:11]
	v_lshl_add_u64 v[2:3], v[2:3], 0, v[16:17]
	global_load_dword v45, v[14:15], off
	global_load_dword v46, v[18:19], off
	global_load_dword v47, v[20:21], off
	global_load_dword v48, v[2:3], off
	global_load_dword v49, v4, s[8:9]
	global_load_dword v50, v4, s[8:9] offset:72
	v_cndmask_b32_e64 v2, 8, 6, s[4:5]
	v_add_lshl_u32 v4, v2, v24, 2
	s_mov_b32 s31, 0x800000
	v_lshl_add_u64 v[2:3], s[8:9], 0, v[4:5]
	v_lshl_add_u64 v[8:9], v[2:3], 0, v[8:9]
	v_lshl_add_u64 v[12:13], v[2:3], 0, v[12:13]
	v_lshl_add_u64 v[10:11], v[2:3], 0, v[10:11]
	v_lshl_add_u64 v[2:3], v[2:3], 0, v[16:17]
	v_cmp_gt_u32_e64 s[12:13], 3, v27
	v_cmp_ne_u32_e64 s[14:15], 0, v7
	v_cmp_eq_u32_e64 s[16:17], 3, v7
	s_add_u32 s24, s24, s30
	s_addc_u32 s25, s25, 0
	global_load_dword v15, v4, s[8:9]
	global_load_dword v16, v[8:9], off
	global_load_dword v17, v[12:13], off
	global_load_dword v18, v[10:11], off
	global_load_dword v19, v4, s[8:9] offset:72
	global_load_dword v20, v[2:3], off
	s_mov_b32 s34, 0xe52632a
	v_writelane_b32 v56, s34, 0
	s_mov_b32 s34, 0x2102e45
	v_writelane_b32 v56, s34, 1
	s_mov_b32 s34, 0x1f202f6f
	v_writelane_b32 v56, s34, 2
	s_mov_b32 s34, 0x142d0a56
	v_writelane_b32 v56, s34, 3
	s_mov_b32 s34, 0x2b1c1160
	v_writelane_b32 v56, s34, 4
	s_mov_b32 s34, 0x47394854
	v_writelane_b32 v56, s34, 5
	s_mov_b32 s34, 0x12071303
	v_writelane_b32 v56, s34, 6
	s_mov_b32 s34, 0x15746465
	v_writelane_b32 v56, s34, 7
	s_mov_b32 s34, 0x2b5a3e22
	v_writelane_b32 v56, s34, 8
	s_mov_b32 s34, 0x34176831
	v_writelane_b32 v56, s34, 9
	s_mov_b32 s34, 0x50354d33
	v_writelane_b32 v56, s34, 10
	s_mov_b32 s34, 0x1b43114f
	v_writelane_b32 v56, s34, 11
	s_mov_b32 s34, 0x3d66413c
	v_writelane_b32 v56, s34, 12
	s_mov_b32 s34, 0x9235c30
	v_writelane_b32 v56, s34, 13
	s_mov_b32 s34, 0x40695d59
	v_writelane_b32 v56, s34, 14
	s_mov_b32 s34, 0x5e361a4e
	v_writelane_b32 v56, s34, 15
	s_mov_b32 s34, 0x1441d
	v_writelane_b32 v56, s34, 16
	s_mov_b32 s34, 0x46625370
	v_writelane_b32 v56, s34, 17
	s_mov_b32 s34, 0x572c1e3b
	v_writelane_b32 v56, s34, 18
	s_mov_b32 s34, 0x72054b4a
	v_writelane_b32 v56, s34, 19
	s_mov_b32 s34, 0xf37616e
	v_writelane_b32 v56, s34, 20
	s_mov_b32 s34, 0x4376171
	v_writelane_b32 v56, s34, 21
	s_mov_b32 s34, 0x49373821
	v_writelane_b32 v56, s34, 22
	s_mov_b32 s34, 0x4c735516
	v_writelane_b32 v56, s34, 23
	s_mov_b32 s34, 0x25763a77
	v_writelane_b32 v56, s34, 24
	s_mov_b32 s34, 0x266a5827
	v_writelane_b32 v56, s34, 25
	s_mov_b32 s34, 0x190b676c
	v_writelane_b32 v56, s34, 26
	s_mov_b32 s34, 0xd51296d
	v_writelane_b32 v56, s34, 27
	s_mov_b32 s34, 0x8067524
	v_writelane_b32 v56, s34, 28
	s_mov_b32 s34, 0x323f4418
	v_writelane_b32 v56, s34, 29
	s_mov_b32 s34, 0x5b780c42
	v_writelane_b32 v56, s34, 30
	s_mov_b32 s34, 0x6b285f1d
	v_writelane_b32 v56, s34, 31
	s_mov_b32 s34, 0x38587000
	v_writelane_b32 v57, s34, 0
	s_mov_b32 s34, 0xa878
	v_writelane_b32 v58, s34, 0
	s_mov_b32 s34, 0x80482830
	v_writelane_b32 v57, s34, 1
	s_mov_b32 s34, 0xa068
	v_writelane_b32 v58, s34, 1
	s_mov_b32 s34, 0x59790191
	v_writelane_b32 v57, s34, 2
	s_mov_b32 s34, 0x3971
	v_writelane_b32 v58, s34, 2
	s_mov_b32 s34, 0x9949515a
	v_writelane_b32 v57, s34, 3
	s_mov_b32 s34, 0x2969
	v_writelane_b32 v58, s34, 3
	s_mov_b32 s34, 0x222422a
	v_writelane_b32 v57, s34, 4
	s_mov_b32 s34, 0x3a72
	v_writelane_b32 v58, s34, 4
	s_mov_b32 s34, 0x329a1a03
	v_writelane_b32 v57, s34, 5
	s_mov_b32 s34, 0x8a6a
	v_writelane_b32 v58, s34, 5
	s_mov_b32 s34, 0x5b23934b
	v_writelane_b32 v57, s34, 6
	s_mov_b32 s34, 0x3b73
	v_writelane_b32 v58, s34, 6
	s_mov_b32 s34, 0x83541374
	v_writelane_b32 v57, s34, 7
	s_mov_b32 s34, 0x336b
	v_writelane_b32 v58, s34, 7
	s_mov_b32 s34, 0x3c1c2434
	v_writelane_b32 v57, s34, 8
	s_mov_b32 s34, 0x48c
	v_writelane_b32 v58, s34, 8
	s_mov_b32 s34, 0x4c1da455
	v_writelane_b32 v57, s34, 9
	s_mov_b32 s34, 0x449c
	v_writelane_b32 v58, s34, 9
	s_mov_b32 s34, 0x8d25052d
	v_writelane_b32 v57, s34, 10
	s_mov_b32 s34, 0x9d5d
	v_writelane_b32 v58, s34, 10
	s_mov_b32 s34, 0x761e4556
	v_writelane_b32 v57, s34, 11
	s_mov_b32 s34, 0x3565
	v_writelane_b32 v58, s34, 11
	s_mov_b32 s34, 0x46368e6e
	v_writelane_b32 v57, s34, 12
	s_mov_b32 s34, 0x63e
	v_writelane_b32 v58, s34, 12
	s_mov_b32 s34, 0x5f579e77
	v_writelane_b32 v57, s34, 13
	s_mov_b32 s34, 0x2ea6
	v_writelane_b32 v58, s34, 13
	s_mov_b32 s34, 0x174f1f9f
	v_writelane_b32 v57, s34, 14
	s_mov_b32 s34, 0x278f
	v_writelane_b32 v58, s34, 14
	s_mov_b32 s34, 0x38584700
	v_writelane_b32 v57, s34, 15
	s_mov_b32 s34, 0xa897
	v_writelane_b32 v58, s34, 15
	s_mov_b32 s34, 0x90982008
	v_writelane_b32 v57, s34, 16
	s_mov_b32 s34, 0x4060
	v_writelane_b32 v58, s34, 16
	s_mov_b32 s34, 0x411810a1
	v_writelane_b32 v57, s34, 17
	s_mov_b32 s34, 0x5088
	v_writelane_b32 v58, s34, 17
	s_mov_b32 s34, 0x8161197a
	v_writelane_b32 v57, s34, 18
	s_mov_b32 s34, 0x2109
	v_writelane_b32 v58, s34, 18
	s_mov_b32 s34, 0x12314aa2
	v_writelane_b32 v57, s34, 19
	s_mov_b32 s34, 0x1189
	v_writelane_b32 v58, s34, 19
	s_mov_b32 s34, 0x520a430b
	v_writelane_b32 v57, s34, 20
	s_mov_b32 s34, 0x6292
	v_writelane_b32 v58, s34, 20
	s_mov_b32 s34, 0x9b828b53
	v_writelane_b32 v57, s34, 21
	s_mov_b32 s34, 0x2b63
	v_writelane_b32 v58, s34, 21
	s_mov_b32 s34, 0x7c7b5c84
	v_writelane_b32 v57, s34, 22
	s_mov_b32 s34, 0xa31b
	v_writelane_b32 v58, s34, 22
	s_mov_b32 s34, 0x6c0c957d
	v_writelane_b32 v57, s34, 23
	s_mov_b32 s34, 0x942c
	v_writelane_b32 v58, s34, 23
	s_mov_b32 s34, 0x753d85a5
	v_writelane_b32 v57, s34, 24
	s_mov_b32 s34, 0x6414
	v_writelane_b32 v58, s34, 24
	s_mov_b32 s34, 0x5e6d7e26
	v_writelane_b32 v57, s34, 25
	s_mov_b32 s34, 0x4d0d
	v_writelane_b32 v58, s34, 25
	s_mov_b32 s34, 0x8666160f
	v_writelane_b32 v57, s34, 26
	s_mov_b32 s34, 0x9615
	v_writelane_b32 v58, s34, 26
	s_mov_b32 s34, 0x2f7f0787
	v_writelane_b32 v57, s34, 27
	s_mov_b32 s34, 0x4e0e
	v_writelane_b32 v58, s34, 27
	s_mov_b32 s34, 0xa76f2008
	v_writelane_b32 v57, s34, 28
	s_mov_b32 s34, 0x373f
	v_writelane_b32 v58, s34, 28
	s_mov_b32 s34, 0x90982008
	v_writelane_b32 v57, s34, 29
	s_mov_b32 s34, 0x4067
	v_writelane_b32 v58, s34, 29
	s_mov_b32 s34, 0x90982008
	v_writelane_b32 v57, s34, 30
	s_mov_b32 s34, 0x4060
	v_writelane_b32 v58, s34, 30
	s_mov_b32 s34, 0x90982008
	v_writelane_b32 v57, s34, 31
	s_mov_b32 s34, 0x4060
	v_writelane_b32 v58, s34, 31
	s_waitcnt vmcnt(30)
	v_add_f32_e32 v59, 0x3727c5ac, v23
	v_mul_f32_e32 v21, 0x4b800000, v59
	v_cmp_gt_f32_e64 s[6:7], s31, v59
	s_nop 1
	v_cndmask_b32_e64 v59, v59, v21, s[6:7]
	v_rsq_f32_e32 v59, v59
	v_cmp_gt_u32_e64 s[8:9], 3, v26
	v_mul_f32_e32 v2, 0x45800000, v59
	v_cndmask_b32_e64 v2, v59, v2, s[6:7]
	v_mul_f32_e32 v12, v22, v2
	v_cmp_eq_u32_e64 s[6:7], 0, v7
	s_waitcnt vmcnt(29)
	v_fma_mixlo_f16 v2, v12, v25, 0
	s_waitcnt vmcnt(28)
	v_fma_mixlo_f16 v3, v12, v28, 0
	v_cndmask_b32_e64 v8, 0, v3, s[8:9]
	s_waitcnt vmcnt(26)
	v_fma_mixlo_f16 v4, v12, v30, 0
	v_fma_mixlo_f16 v3, v12, v29, 0
	v_cndmask_b32_e64 v2, 0, v2, s[6:7]
	v_cndmask_b32_e32 v4, 0, v4, vcc
	v_cndmask_b32_e64 v3, 0, v3, s[12:13]
	v_pack_b32_f16 v2, v2, v8
	v_lshlrev_b32_e32 v8, 4, v0
	s_waitcnt vmcnt(25)
	v_fma_mixlo_f16 v9, v12, v31, 0
	s_waitcnt vmcnt(24)
	v_fma_mixlo_f16 v10, v12, v32, 0
	v_cndmask_b32_e64 v9, 0, v9, s[14:15]
	v_cndmask_b32_e64 v7, 0, v10, s[16:17]
	v_pack_b32_f16 v4, v4, v7
	v_pack_b32_f16 v3, v3, v9
	v_mov_b32_e32 v9, v5
	global_store_dwordx4 v8, v[2:5], s[24:25]
	v_lshl_add_u64 v[10:11], s[24:25], 0, v[8:9]
	s_waitcnt vmcnt(19)
	v_fma_mixlo_f16 v13, v12, v38, 0
	v_fma_mixlo_f16 v3, v12, v34, 0
	v_fma_mixlo_f16 v4, v12, v36, 0
	v_fma_mixlo_f16 v2, v12, v33, 0
	v_cndmask_b32_e64 v7, 0, v3, s[8:9]
	v_fma_mixlo_f16 v3, v12, v35, 0
	v_cndmask_b32_e64 v9, 0, v4, s[14:15]
	v_fma_mixlo_f16 v4, v12, v37, 0
	v_cndmask_b32_e64 v2, 0, v2, s[6:7]
	v_cndmask_b32_e64 v3, 0, v3, s[12:13]
	v_cndmask_b32_e32 v4, 0, v4, vcc
	v_cndmask_b32_e64 v13, 0, v13, s[16:17]
	v_pack_b32_f16 v4, v4, v13
	v_pack_b32_f16 v3, v3, v9
	v_pack_b32_f16 v2, v2, v7
	global_store_dwordx4 v8, v[2:5], s[24:25] offset:1024
	s_waitcnt vmcnt(14)
	v_fma_mixlo_f16 v13, v12, v44, 0
	v_cndmask_b32_e64 v13, 0, v13, s[16:17]
	v_fma_mixlo_f16 v3, v12, v40, 0
	v_fma_mixlo_f16 v4, v12, v42, 0
	v_fma_mixlo_f16 v2, v12, v39, 0
	v_cndmask_b32_e64 v7, 0, v3, s[8:9]
	v_fma_mixlo_f16 v3, v12, v41, 0
	v_cndmask_b32_e64 v9, 0, v4, s[14:15]
	v_fma_mixlo_f16 v4, v12, v43, 0
	v_cndmask_b32_e64 v2, 0, v2, s[6:7]
	v_cndmask_b32_e64 v3, 0, v3, s[12:13]
	v_cndmask_b32_e32 v4, 0, v4, vcc
	v_pack_b32_f16 v4, v4, v13
	v_pack_b32_f16 v3, v3, v9
	v_pack_b32_f16 v2, v2, v7
	global_store_dwordx4 v8, v[2:5], s[24:25] offset:2048
	s_waitcnt vmcnt(9)
	v_fma_mixlo_f16 v13, v12, v50, 0
	v_cndmask_b32_e64 v13, 0, v13, s[16:17]
	v_fma_mixlo_f16 v3, v12, v45, 0
	v_fma_mixlo_f16 v4, v12, v47, 0
	v_fma_mixlo_f16 v2, v12, v49, 0
	v_cndmask_b32_e64 v7, 0, v3, s[8:9]
	v_fma_mixlo_f16 v3, v12, v46, 0
	v_cndmask_b32_e64 v9, 0, v4, s[14:15]
	v_fma_mixlo_f16 v4, v12, v48, 0
	v_cndmask_b32_e64 v2, 0, v2, s[6:7]
	v_cndmask_b32_e64 v3, 0, v3, s[12:13]
	v_cndmask_b32_e32 v4, 0, v4, vcc
	v_pack_b32_f16 v4, v4, v13
	v_pack_b32_f16 v3, v3, v9
	v_pack_b32_f16 v2, v2, v7
	global_store_dwordx4 v8, v[2:5], s[24:25] offset:3072
	s_and_b64 vcc, s[4:5], vcc
	s_nop 0
	v_and_b32_e32 v2, 35, v0
	s_waitcnt vmcnt(9)
	v_fma_mixlo_f16 v3, v12, v15, 0
	v_cmp_eq_u32_e64 s[6:7], 0, v2
	s_waitcnt vmcnt(6)
	v_fma_mixlo_f16 v4, v12, v18, 0
	v_cndmask_b32_e64 v7, 0, v3, s[6:7]
	v_fma_mixlo_f16 v3, v12, v16, 0
	s_and_b64 s[6:7], s[4:5], s[8:9]
	v_cndmask_b32_e64 v8, 0, v3, s[6:7]
	v_fma_mixlo_f16 v3, v12, v17, 0
	s_and_b64 s[6:7], s[4:5], s[12:13]
	v_cndmask_b32_e64 v3, 0, v3, s[6:7]
	s_and_b64 s[6:7], s[4:5], s[14:15]
	v_cndmask_b32_e64 v9, 0, v4, s[6:7]
	s_waitcnt vmcnt(4)
	v_fma_mixlo_f16 v4, v12, v20, 0
	v_cndmask_b32_e32 v4, 0, v4, vcc
	v_fma_mixlo_f16 v12, v12, v19, 0
	v_cmp_eq_u32_e32 vcc, 3, v2
	v_pack_b32_f16 v3, v3, v9
	s_nop 0
	v_cndmask_b32_e32 v2, 0, v12, vcc
	v_pack_b32_f16 v4, v4, v2
	v_pack_b32_f16 v2, v7, v8
	v_add_co_u32_e32 v8, vcc, 0x1000, v10
	s_nop 1
	v_addc_co_u32_e32 v9, vcc, 0, v11, vcc
	v_cmp_gt_u32_e32 vcc, 8, v0
	global_store_dwordx4 v[8:9], v[2:5], off
	s_and_saveexec_b64 s[4:5], vcc
	s_cbranch_execz .LBB0_7
	s_add_u32 s6, s26, s30
	s_addc_u32 s7, s27, 0
	v_add_f32_e32 v2, 0x3727c5ac, v52
	v_mul_f32_e32 v3, 0x4b800000, v2
	v_cmp_gt_f32_e32 vcc, s31, v2
	s_nop 1
	v_cndmask_b32_e32 v2, v2, v3, vcc
	v_rsq_f32_e32 v2, v2
	v_sub_f32_e32 v3, v53, v54
	v_mul_f32_e32 v4, 0x45800000, v2
	v_cndmask_b32_e32 v2, v2, v4, vcc
	v_mul_f32_e32 v2, v51, v2
	v_fmac_f32_e32 v55, v3, v2
	v_lshlrev_b32_e32 v2, 2, v0
	global_store_dword v2, v55, s[6:7]

.LBB0_11:
	s_andn2_b64 vcc, exec, s[4:5]
	s_cbranch_vccnz .LBB0_45
	v_lshlrev_b32_e32 v28, 2, v1
	s_cmpk_gt_u32 s2, 0x23f
	s_cbranch_scc0 .LBB0_18
	s_add_i32 s6, s3, 0xffffffb8
	s_mul_hi_u32 s7, s6, 0x88888889
	s_lshr_b32 s12, s7, 3
	s_mul_i32 s7, s12, 15
	s_sub_i32 s6, s6, s7
	s_and_b32 s7, s6, 0xff
	s_mulk_i32 s7, 0xcd
	s_lshr_b32 s13, s7, 10
	s_mul_i32 s7, s13, 5
	s_sub_i32 s14, s6, s7
	v_cmp_lt_u32_e32 vcc, 31, v0
	s_and_saveexec_b64 s[6:7], vcc
	s_xor_b64 s[6:7], exec, s[6:7]
	s_cbranch_execz .LBB0_26
	s_and_b32 s8, s14, 0xff
	s_cmp_lt_i32 s8, 1
	s_mov_b32 s15, 1
	s_cbranch_scc1 .LBB0_26
	s_and_b32 s9, 0xffff, s8
	s_cmp_lt_i32 s9, 2
	s_cbranch_scc1 .LBB0_19
	s_cmp_eq_u32 s9, 2
	s_cbranch_scc1 .LBB0_20
	s_cmp_eq_u32 s8, 3
	s_cselect_b32 s15, 5, 9
	s_mov_b64 s[8:9], 0
	s_branch .LBB0_21

.LBB0_42:
	v_cmp_gt_u32_e32 vcc, 9, v2
	s_movk_i32 s8, 0xe0
	v_mad_u32_u24 v6, v1, s8, v13
	v_cndmask_b32_e32 v2, 0, v2, vcc
	v_mad_u64_u32 v[14:15], s[6:7], v6, 9, v[2:3]
	v_mad_u32_u24 v6, v1, s8, v12
	v_mad_u64_u32 v[12:13], s[6:7], v6, 9, v[2:3]
	v_ashrrev_i32_e32 v13, 31, v12
	v_mad_u32_u24 v6, v1, s8, v9
	s_waitcnt lgkmcnt(0)
	global_load_dword v10, v28, s[42:43]
	global_load_dword v11, v28, s[44:45]
	v_lshl_add_u64 v[16:17], v[12:13], 2, s[40:41]
	v_mad_u64_u32 v[12:13], s[6:7], v6, 9, v[2:3]
	v_mad_u32_u24 v6, v1, s8, v8
	v_mad_u64_u32 v[8:9], s[6:7], v6, 9, v[2:3]
	v_mad_u32_u24 v6, v1, s8, v7
	v_mad_u64_u32 v[6:7], s[6:7], v6, 9, v[2:3]
	v_ashrrev_i32_e32 v7, 31, v6
	v_mad_u32_u24 v5, v1, s8, v5
	v_mad_u32_u24 v4, v1, s8, v4
	v_mad_u32_u24 v1, v1, s8, v3
	v_ashrrev_i32_e32 v15, 31, v14
	v_lshl_add_u64 v[22:23], v[6:7], 2, s[40:41]
	v_mad_u64_u32 v[6:7], s[6:7], v5, 9, v[2:3]
	v_mad_u64_u32 v[4:5], s[6:7], v4, 9, v[2:3]
	v_mad_u64_u32 v[2:3], s[6:7], v1, 9, v[2:3]
	v_lshl_add_u64 v[14:15], v[14:15], 2, s[40:41]
	v_ashrrev_i32_e32 v13, 31, v12
	v_ashrrev_i32_e32 v9, 31, v8
	v_ashrrev_i32_e32 v7, 31, v6
	v_ashrrev_i32_e32 v5, 31, v4
	v_ashrrev_i32_e32 v3, 31, v2
	v_lshl_add_u64 v[18:19], v[12:13], 2, s[40:41]
	v_lshl_add_u64 v[20:21], v[8:9], 2, s[40:41]
	v_lshl_add_u64 v[24:25], v[6:7], 2, s[40:41]
	v_lshl_add_u64 v[26:27], v[4:5], 2, s[40:41]
	v_lshl_add_u64 v[2:3], v[2:3], 2, s[40:41]
	global_load_dword v12, v[14:15], off
	global_load_dword v8, v[16:17], off
	global_load_dword v9, v[18:19], off
	global_load_dword v6, v[20:21], off
	global_load_dword v7, v[22:23], off
	global_load_dword v4, v[24:25], off
	global_load_dword v5, v[26:27], off
	global_load_dword v1, v[2:3], off
	s_and_b64 s[6:7], s[10:11], vcc
	v_mov_b32_e32 v3, 0
	v_mov_b32_e32 v2, 0
	s_and_saveexec_b64 s[4:5], s[6:7]
	s_cbranch_execz .LBB0_44
	s_waitcnt vmcnt(8)
	v_add_f32_e32 v2, 0x3727c5ac, v11
	s_mov_b32 s6, 0x800000
	v_mul_f32_e32 v11, 0x4b800000, v2
	v_cmp_gt_f32_e32 vcc, s6, v2
	s_nop 1
	v_cndmask_b32_e32 v2, v2, v11, vcc
	v_rsq_f32_e32 v2, v2
	s_nop 0
	v_mul_f32_e32 v11, 0x45800000, v2
	v_cndmask_b32_e32 v2, v2, v11, vcc
	v_mul_f32_e32 v2, v10, v2

	.amdhsa_kernel _Z6k_prepPKfS0_S0_S0_S0_S0_S0_S0_S0_S0_S0_S0_S0_PDv8_DF16_S2_S2_PfS0_
		.amdhsa_group_segment_fixed_size 0
		.amdhsa_private_segment_fixed_size 0
		.amdhsa_kernarg_size 144
		.amdhsa_user_sgpr_count 2
		.amdhsa_user_sgpr_dispatch_ptr 0
		.amdhsa_user_sgpr_queue_ptr 0
		.amdhsa_user_sgpr_kernarg_segment_ptr 1
		.amdhsa_user_sgpr_dispatch_id 0
		.amdhsa_user_sgpr_kernarg_preload_length 0
		.amdhsa_user_sgpr_kernarg_preload_offset 0
		.amdhsa_user_sgpr_private_segment_size 0
		.amdhsa_uses_dynamic_stack 0
		.amdhsa_enable_private_segment 0
		.amdhsa_system_sgpr_workgroup_id_x 1
		.amdhsa_system_sgpr_workgroup_id_y 0
		.amdhsa_system_sgpr_workgroup_id_z 0
		.amdhsa_system_sgpr_workgroup_info 0
		.amdhsa_system_vgpr_workitem_id 0
		.amdhsa_next_free_vgpr 60
		.amdhsa_next_free_sgpr 48
		.amdhsa_accum_offset 60
		.amdhsa_reserve_vcc 1
		.amdhsa_float_round_mode_32 0
		.amdhsa_float_round_mode_16_64 0
		.amdhsa_float_denorm_mode_32 3
		.amdhsa_float_denorm_mode_16_64 3
		.amdhsa_dx10_clamp 1
		.amdhsa_ieee_mode 1
		.amdhsa_fp16_overflow 0
		.amdhsa_tg_split 0
		.amdhsa_exception_fp_ieee_invalid_op 0
		.amdhsa_exception_fp_denorm_src 0
		.amdhsa_exception_fp_ieee_div_zero 0
		.amdhsa_exception_fp_ieee_overflow 0
		.amdhsa_exception_fp_ieee_underflow 0
		.amdhsa_exception_fp_ieee_inexact 0
		.amdhsa_exception_int_div_zero 0
	.end_amdhsa_kernel

amdhsa.kernels:
  - .agpr_count:     0
    .args:
      - .actual_access:  read_only
        .address_space:  global
        .offset:         0
        .size:           8
        .value_kind:     global_buffer
      - .actual_access:  read_only
        .address_space:  global
        .offset:         8
        .size:           8
        .value_kind:     global_buffer
      - .actual_access:  read_only
        .address_space:  global
        .offset:         16
        .size:           8
        .value_kind:     global_buffer
      - .actual_access:  read_only
        .address_space:  global
        .offset:         24
        .size:           8
        .value_kind:     global_buffer
      - .actual_access:  read_only
        .address_space:  global
        .offset:         32
        .size:           8
        .value_kind:     global_buffer
      - .actual_access:  read_only
        .address_space:  global
        .offset:         40
        .size:           8
        .value_kind:     global_buffer
      - .actual_access:  read_only
        .address_space:  global
        .offset:         48
        .size:           8
        .value_kind:     global_buffer
      - .actual_access:  read_only
        .address_space:  global
        .offset:         56
        .size:           8
        .value_kind:     global_buffer
      - .actual_access:  read_only
        .address_space:  global
        .offset:         64
        .size:           8
        .value_kind:     global_buffer
      - .actual_access:  read_only
        .address_space:  global
        .offset:         72
        .size:           8
        .value_kind:     global_buffer
      - .actual_access:  read_only
        .address_space:  global
        .offset:         80
        .size:           8
        .value_kind:     global_buffer
      - .actual_access:  read_only
        .address_space:  global
        .offset:         88
        .size:           8
        .value_kind:     global_buffer
      - .actual_access:  read_only
        .address_space:  global
        .offset:         96
        .size:           8
        .value_kind:     global_buffer
      - .address_space:  global
        .offset:         104
        .size:           8
        .value_kind:     global_buffer
      - .address_space:  global
        .offset:         112
        .size:           8
        .value_kind:     global_buffer
      - .address_space:  global
        .offset:         120
        .size:           8
        .value_kind:     global_buffer
      - .address_space:  global
        .offset:         128
        .size:           8
        .value_kind:     global_buffer
      - .actual_access:  read_only
        .address_space:  global
        .offset:         136
        .size:           8
        .value_kind:     global_buffer
    .group_segment_fixed_size: 0
    .kernarg_segment_align: 8
    .kernarg_segment_size: 144
    .language:       OpenCL C
    .language_version:
      - 2
      - 0
    .max_flat_workgroup_size: 64
    .name:           _Z6k_prepPKfS0_S0_S0_S0_S0_S0_S0_S0_S0_S0_S0_S0_PDv8_DF16_S2_S2_PfS0_
    .private_segment_fixed_size: 0
    .sgpr_count:     54
    .sgpr_spill_count: 0
    .symbol:         _Z6k_prepPKfS0_S0_S0_S0_S0_S0_S0_S0_S0_S0_S0_S0_PDv8_DF16_S2_S2_PfS0_.kd
    .uniform_work_group_size: 1
    .uses_dynamic_stack: false
    .vgpr_count:     60
    .vgpr_spill_count: 0
    .wavefront_size: 64
  - .agpr_count:     0
    .args:
      - .actual_access:  read_only
        .address_space:  global
        .offset:         0
        .size:           8
        .value_kind:     global_buffer
      - .address_space:  global
        .offset:         8
        .size:           8
        .value_kind:     global_buffer
      - .address_space:  global
        .offset:         16
        .size:           8
        .value_kind:     global_buffer
      - .address_space:  global
        .offset:         24
        .size:           8
        .value_kind:     global_buffer
      - .actual_access:  read_only
        .address_space:  global
        .offset:         32
        .size:           8
        .value_kind:     global_buffer
      - .actual_access:  read_only
        .address_space:  global
        .offset:         40
        .size:           8
        .value_kind:     global_buffer
      - .actual_access:  read_only
        .address_space:  global
        .offset:         48
        .size:           8
        .value_kind:     global_buffer
      - .actual_access:  read_only
        .address_space:  global
        .offset:         56
        .size:           8
        .value_kind:     global_buffer
      - .actual_access:  read_only
        .address_space:  global
        .offset:         64
        .size:           8
        .value_kind:     global_buffer
      - .actual_access:  read_only
        .address_space:  global
        .offset:         72
        .size:           8
        .value_kind:     global_buffer
      - .actual_access:  read_only
        .address_space:  global
        .offset:         80
        .size:           8
        .value_kind:     global_buffer
      - .actual_access:  read_only
        .address_space:  global
        .offset:         88
        .size:           8
        .value_kind:     global_buffer
      - .actual_access:  read_only
        .address_space:  global
        .offset:         96
        .size:           8
        .value_kind:     global_buffer
      - .address_space:  global
        .offset:         104
        .size:           8
        .value_kind:     global_buffer
      - .actual_access:  read_only
        .address_space:  global
        .offset:         112
        .size:           8
        .value_kind:     global_buffer
      - .actual_access:  read_only
        .address_space:  global
        .offset:         120
        .size:           8
        .value_kind:     global_buffer
      - .actual_access:  read_only
        .address_space:  global
        .offset:         128
        .size:           8
        .value_kind:     global_buffer
      - .actual_access:  read_only
        .address_space:  global
        .offset:         136
        .size:           8
        .value_kind:     global_buffer
      - .actual_access:  read_only
        .address_space:  global
        .offset:         144
        .size:           8
        .value_kind:     global_buffer
      - .actual_access:  read_only
        .address_space:  global
        .offset:         152
        .size:           8
        .value_kind:     global_buffer
      - .actual_access:  read_only
        .address_space:  global
        .offset:         160
        .size:           8
        .value_kind:     global_buffer
      - .actual_access:  read_only
        .address_space:  global
        .offset:         168
        .size:           8
        .value_kind:     global_buffer
      - .actual_access:  read_only
        .address_space:  global
        .offset:         176
        .size:           8
        .value_kind:     global_buffer
      - .actual_access:  read_only
        .address_space:  global
        .offset:         184
        .size:           8
        .value_kind:     global_buffer
      - .actual_access:  read_only
        .address_space:  global
        .offset:         192
        .size:           8
        .value_kind:     global_buffer
      - .actual_access:  read_only
        .address_space:  global
        .offset:         200
        .size:           8
        .value_kind:     global_buffer
      - .actual_access:  read_only
        .address_space:  global
        .offset:         208
        .size:           8
        .value_kind:     global_buffer
      - .actual_access:  write_only
        .address_space:  global
        .offset:         216
        .size:           8
        .value_kind:     global_buffer
    .group_segment_fixed_size: 78032
    .kernarg_segment_align: 8
    .kernarg_segment_size: 224
    .language:       OpenCL C
    .language_version:
      - 2
      - 0
    .max_flat_workgroup_size: 512
    .name:           _Z6k_mainPKfPKDv8_DF16_S0_S3_S0_S0_S0_S0_S0_S0_S0_S0_S0_S3_S0_S0_S0_S0_S0_S0_S0_S0_S0_S0_S0_S0_S0_Pf
    .private_segment_fixed_size: 0
    .sgpr_count:     78
    .sgpr_spill_count: 0
    .symbol:         _Z6k_mainPKfPKDv8_DF16_S0_S3_S0_S0_S0_S0_S0_S0_S0_S0_S0_S3_S0_S0_S0_S0_S0_S0_S0_S0_S0_S0_S0_S0_S0_Pf.kd
    .uniform_work_group_size: 1
    .uses_dynamic_stack: false
    .vgpr_count:     128
    .vgpr_spill_count: 0
    .wavefront_size: 64
